# speedup vs baseline: 1.0334x; 1.0246x over previous
.LBB1_82:
	ds_read_b128 v[130:133], v219 offset:32768
	ds_read_b128 v[134:137], v219 offset:33792
	ds_read_b128 v[138:141], v219 offset:34816
	ds_read_b128 v[142:145], v219 offset:35840
	ds_read_b128 v[178:181], v219 offset:49152
	ds_read_b128 v[182:185], v219 offset:50176
	ds_read_b128 v[186:189], v219 offset:51200
	ds_read_b128 v[190:193], v219 offset:52224
	ds_read_b128 v[146:149], v220
	ds_read_b128 v[150:153], v220 offset:1024
	ds_read_b128 v[154:157], v221
	ds_read_b128 v[158:161], v221 offset:1024
	ds_read_b128 v[162:165], v222
	ds_read_b128 v[166:169], v222 offset:1024
	ds_read_b128 v[170:173], v223
	ds_read_b128 v[174:177], v223 offset:1024
	s_setprio 2
	s_add_i32 s12, s8, 1
	v_readlane_b32 s9, v248, s12
	s_mov_b32 m0, s43
	s_nop 1
	v_add_u32_e32 v251, s9, v249
	global_load_lds_dwordx4 v251, s[18:19]
	v_add_u32_e32 v251, s9, v250
	s_mov_b32 m0, s44
	s_nop 0
	global_load_lds_dwordx4 v251, s[18:19]
	s_setprio 0
	s_waitcnt vmcnt(8) lgkmcnt(0)
	s_barrier
	s_setprio 1
	v_mfma_f32_16x16x32_f16 v[124:127], v[130:133], v[146:149], v[124:127]
	v_mfma_f32_16x16x32_f16 v[120:123], v[138:141], v[146:149], v[120:123]
	v_mfma_f32_16x16x32_f16 v[116:119], v[130:133], v[154:157], v[116:119]
	v_mfma_f32_16x16x32_f16 v[112:115], v[138:141], v[154:157], v[112:115]
	v_mfma_f32_16x16x32_f16 v[108:111], v[130:133], v[162:165], v[108:111]
	v_mfma_f32_16x16x32_f16 v[104:107], v[138:141], v[162:165], v[104:107]
	v_mfma_f32_16x16x32_f16 v[100:103], v[130:133], v[170:173], v[100:103]
	v_mfma_f32_16x16x32_f16 v[96:99], v[138:141], v[170:173], v[96:99]
	v_mfma_f32_16x16x32_f16 v[124:127], v[134:137], v[150:153], v[124:127]
	v_mfma_f32_16x16x32_f16 v[120:123], v[142:145], v[150:153], v[120:123]
	v_mfma_f32_16x16x32_f16 v[116:119], v[134:137], v[158:161], v[116:119]
	v_mfma_f32_16x16x32_f16 v[112:115], v[142:145], v[158:161], v[112:115]
	v_mfma_f32_16x16x32_f16 v[108:111], v[134:137], v[166:169], v[108:111]
	v_mfma_f32_16x16x32_f16 v[104:107], v[142:145], v[166:169], v[104:107]
	v_mfma_f32_16x16x32_f16 v[100:103], v[134:137], v[174:177], v[100:103]
	v_mfma_f32_16x16x32_f16 v[96:99], v[142:145], v[174:177], v[96:99]
	v_mfma_f32_16x16x32_f16 v[52:55], v[178:181], v[146:149], v[52:55]
	v_mfma_f32_16x16x32_f16 v[40:43], v[186:189], v[146:149], v[40:43]
	v_mfma_f32_16x16x32_f16 v[36:39], v[178:181], v[154:157], v[36:39]
	v_mfma_f32_16x16x32_f16 v[32:35], v[186:189], v[154:157], v[32:35]
	v_mfma_f32_16x16x32_f16 v[28:31], v[178:181], v[162:165], v[28:31]
	v_mfma_f32_16x16x32_f16 v[24:27], v[186:189], v[162:165], v[24:27]
	v_mfma_f32_16x16x32_f16 v[20:23], v[178:181], v[170:173], v[20:23]
	v_mfma_f32_16x16x32_f16 v[16:19], v[186:189], v[170:173], v[16:19]
	v_mfma_f32_16x16x32_f16 v[52:55], v[182:185], v[150:153], v[52:55]
	v_mfma_f32_16x16x32_f16 v[40:43], v[190:193], v[150:153], v[40:43]
	v_mfma_f32_16x16x32_f16 v[36:39], v[182:185], v[158:161], v[36:39]
	v_mfma_f32_16x16x32_f16 v[32:35], v[190:193], v[158:161], v[32:35]
	v_mfma_f32_16x16x32_f16 v[28:31], v[182:185], v[166:169], v[28:31]
	v_mfma_f32_16x16x32_f16 v[24:27], v[190:193], v[166:169], v[24:27]
	v_mfma_f32_16x16x32_f16 v[20:23], v[182:185], v[174:177], v[20:23]
	v_mfma_f32_16x16x32_f16 v[16:19], v[190:193], v[174:177], v[16:19]
	s_setprio 0
	s_barrier
	ds_read_b128 v[146:149], v220 offset:16384
	ds_read_b128 v[150:153], v220 offset:17408
	ds_read_b128 v[154:157], v221 offset:16384
	ds_read_b128 v[158:161], v221 offset:17408
	ds_read_b128 v[162:165], v222 offset:16384
	ds_read_b128 v[166:169], v222 offset:17408
	ds_read_b128 v[170:173], v223 offset:16384
	ds_read_b128 v[174:177], v223 offset:17408
	s_setprio 2
	v_add_u32_e32 v129, s7, v128
	s_mov_b32 m0, s22
	v_add_u32_e32 v194, 0xffffff80, v129
	global_load_lds_dwordx4 v194, s[10:11]
	v_add_u32_e32 v194, 0x47f80, v129
	s_mov_b32 m0, s23
	s_add_i32 s9, s8, 2
	global_load_lds_dwordx4 v194, s[10:11]
	v_readlane_b32 s13, v248, s9
	s_mov_b32 m0, s21
	s_nop 1
	v_add_u32_e32 v194, s13, v206
	global_load_lds_dwordx4 v194, s[18:19]
	v_add_u32_e32 v194, s13, v213
	s_mov_b32 m0, s24
	s_nop 0
	global_load_lds_dwordx4 v194, s[18:19]
	s_mov_b32 m0, s25
	v_add_u32_e32 v194, 0x8ff80, v129
	global_load_lds_dwordx4 v194, s[10:11]
	v_add_u32_e32 v194, 0xd7f80, v129
	s_mov_b32 m0, s26
	s_nop 0
	global_load_lds_dwordx4 v194, s[10:11]
	s_setprio 0
	s_waitcnt vmcnt(8) lgkmcnt(0)
	s_barrier
	s_setprio 1
	v_mfma_f32_16x16x32_f16 v[12:15], v[130:133], v[146:149], v[12:15]
	v_mfma_f32_16x16x32_f16 v[8:11], v[138:141], v[146:149], v[8:11]
	v_mfma_f32_16x16x32_f16 v[4:7], v[130:133], v[154:157], v[4:7]
	v_mfma_f32_16x16x32_f16 v[0:3], v[138:141], v[154:157], v[0:3]
	v_mfma_f32_16x16x32_f16 v[44:47], v[130:133], v[162:165], v[44:47]
	v_mfma_f32_16x16x32_f16 v[48:51], v[138:141], v[162:165], v[48:51]
	v_mfma_f32_16x16x32_f16 v[56:59], v[130:133], v[170:173], v[56:59]
	v_mfma_f32_16x16x32_f16 v[60:63], v[138:141], v[170:173], v[60:63]
	v_mfma_f32_16x16x32_f16 v[12:15], v[134:137], v[150:153], v[12:15]
	v_mfma_f32_16x16x32_f16 v[8:11], v[142:145], v[150:153], v[8:11]
	v_mfma_f32_16x16x32_f16 v[4:7], v[134:137], v[158:161], v[4:7]
	v_mfma_f32_16x16x32_f16 v[0:3], v[142:145], v[158:161], v[0:3]
	v_mfma_f32_16x16x32_f16 v[44:47], v[134:137], v[166:169], v[44:47]
	v_mfma_f32_16x16x32_f16 v[48:51], v[142:145], v[166:169], v[48:51]
	v_mfma_f32_16x16x32_f16 v[56:59], v[134:137], v[174:177], v[56:59]
	v_mfma_f32_16x16x32_f16 v[60:63], v[142:145], v[174:177], v[60:63]
	v_mfma_f32_16x16x32_f16 v[64:67], v[178:181], v[146:149], v[64:67]
	v_mfma_f32_16x16x32_f16 v[68:71], v[186:189], v[146:149], v[68:71]
	v_mfma_f32_16x16x32_f16 v[72:75], v[178:181], v[154:157], v[72:75]
	v_mfma_f32_16x16x32_f16 v[76:79], v[186:189], v[154:157], v[76:79]
	v_mfma_f32_16x16x32_f16 v[80:83], v[178:181], v[162:165], v[80:83]
	v_mfma_f32_16x16x32_f16 v[84:87], v[186:189], v[162:165], v[84:87]
	v_mfma_f32_16x16x32_f16 v[88:91], v[178:181], v[170:173], v[88:91]
	v_mfma_f32_16x16x32_f16 v[92:95], v[186:189], v[170:173], v[92:95]
	v_mfma_f32_16x16x32_f16 v[64:67], v[182:185], v[150:153], v[64:67]
	v_mfma_f32_16x16x32_f16 v[68:71], v[190:193], v[150:153], v[68:71]
	v_mfma_f32_16x16x32_f16 v[72:75], v[182:185], v[158:161], v[72:75]
	v_mfma_f32_16x16x32_f16 v[76:79], v[190:193], v[158:161], v[76:79]
	v_mfma_f32_16x16x32_f16 v[80:83], v[182:185], v[166:169], v[80:83]
	v_mfma_f32_16x16x32_f16 v[84:87], v[190:193], v[166:169], v[84:87]
	v_mfma_f32_16x16x32_f16 v[88:91], v[182:185], v[174:177], v[88:91]
	v_mfma_f32_16x16x32_f16 v[92:95], v[190:193], v[174:177], v[92:95]
	s_setprio 0
	s_barrier
	ds_read_b128 v[130:133], v224
	ds_read_b128 v[134:137], v224 offset:1024
	ds_read_b128 v[138:141], v224 offset:2048
	ds_read_b128 v[142:145], v224 offset:3072
	ds_read_b128 v[178:181], v229
	ds_read_b128 v[182:185], v229 offset:1024
	ds_read_b128 v[186:189], v229 offset:2048
	ds_read_b128 v[190:193], v229 offset:3072
	ds_read_b128 v[146:149], v225
	ds_read_b128 v[150:153], v225 offset:1024
	ds_read_b128 v[154:157], v226
	ds_read_b128 v[158:161], v226 offset:1024
	ds_read_b128 v[162:165], v227
	ds_read_b128 v[166:169], v227 offset:1024
	ds_read_b128 v[170:173], v228
	ds_read_b128 v[174:177], v228 offset:1024
	s_setprio 2
	v_readlane_b32 s12, v248, s9
	s_mov_b32 m0, s27
	s_nop 1
	v_add_u32_e32 v251, s12, v249
	global_load_lds_dwordx4 v251, s[18:19]
	v_add_u32_e32 v251, s12, v250
	s_mov_b32 m0, s28
	s_nop 0
	global_load_lds_dwordx4 v251, s[18:19]
	s_setprio 0
	s_waitcnt vmcnt(8) lgkmcnt(0)
	s_barrier
	s_setprio 1
	v_mfma_f32_16x16x32_f16 v[124:127], v[130:133], v[146:149], v[124:127]
	v_mfma_f32_16x16x32_f16 v[120:123], v[138:141], v[146:149], v[120:123]
	v_mfma_f32_16x16x32_f16 v[116:119], v[130:133], v[154:157], v[116:119]
	v_mfma_f32_16x16x32_f16 v[112:115], v[138:141], v[154:157], v[112:115]
	v_mfma_f32_16x16x32_f16 v[108:111], v[130:133], v[162:165], v[108:111]
	v_mfma_f32_16x16x32_f16 v[104:107], v[138:141], v[162:165], v[104:107]
	v_mfma_f32_16x16x32_f16 v[100:103], v[130:133], v[170:173], v[100:103]
	v_mfma_f32_16x16x32_f16 v[96:99], v[138:141], v[170:173], v[96:99]
	v_mfma_f32_16x16x32_f16 v[124:127], v[134:137], v[150:153], v[124:127]
	v_mfma_f32_16x16x32_f16 v[120:123], v[142:145], v[150:153], v[120:123]
	v_mfma_f32_16x16x32_f16 v[116:119], v[134:137], v[158:161], v[116:119]
	v_mfma_f32_16x16x32_f16 v[112:115], v[142:145], v[158:161], v[112:115]
	v_mfma_f32_16x16x32_f16 v[108:111], v[134:137], v[166:169], v[108:111]
	v_mfma_f32_16x16x32_f16 v[104:107], v[142:145], v[166:169], v[104:107]
	v_mfma_f32_16x16x32_f16 v[100:103], v[134:137], v[174:177], v[100:103]
	v_mfma_f32_16x16x32_f16 v[96:99], v[142:145], v[174:177], v[96:99]
	v_mfma_f32_16x16x32_f16 v[52:55], v[178:181], v[146:149], v[52:55]
	v_mfma_f32_16x16x32_f16 v[40:43], v[186:189], v[146:149], v[40:43]
	v_mfma_f32_16x16x32_f16 v[36:39], v[178:181], v[154:157], v[36:39]
	v_mfma_f32_16x16x32_f16 v[32:35], v[186:189], v[154:157], v[32:35]
	v_mfma_f32_16x16x32_f16 v[28:31], v[178:181], v[162:165], v[28:31]
	v_mfma_f32_16x16x32_f16 v[24:27], v[186:189], v[162:165], v[24:27]
	v_mfma_f32_16x16x32_f16 v[20:23], v[178:181], v[170:173], v[20:23]
	v_mfma_f32_16x16x32_f16 v[16:19], v[186:189], v[170:173], v[16:19]
	v_mfma_f32_16x16x32_f16 v[52:55], v[182:185], v[150:153], v[52:55]
	v_mfma_f32_16x16x32_f16 v[40:43], v[190:193], v[150:153], v[40:43]
	v_mfma_f32_16x16x32_f16 v[36:39], v[182:185], v[158:161], v[36:39]
	v_mfma_f32_16x16x32_f16 v[32:35], v[190:193], v[158:161], v[32:35]
	v_mfma_f32_16x16x32_f16 v[28:31], v[182:185], v[166:169], v[28:31]
	v_mfma_f32_16x16x32_f16 v[24:27], v[190:193], v[166:169], v[24:27]
	v_mfma_f32_16x16x32_f16 v[20:23], v[182:185], v[174:177], v[20:23]
	v_mfma_f32_16x16x32_f16 v[16:19], v[190:193], v[174:177], v[16:19]
	s_setprio 0
	s_barrier
	ds_read_b128 v[146:149], v230
	ds_read_b128 v[150:153], v230 offset:1024
	ds_read_b128 v[154:157], v231
	ds_read_b128 v[158:161], v231 offset:1024
	ds_read_b128 v[162:165], v232
	ds_read_b128 v[166:169], v232 offset:1024
	ds_read_b128 v[170:173], v233
	ds_read_b128 v[174:177], v233 offset:1024
	s_setprio 2
	s_mov_b32 m0, s37
	v_add_u32_e32 v194, 0x48000, v129
	global_load_lds_dwordx4 v129, s[10:11]
	s_mov_b32 m0, s38
	s_add_i32 s12, s8, 3
	global_load_lds_dwordx4 v194, s[10:11]
	v_readlane_b32 s13, v248, s12
	s_mov_b32 m0, s39
	s_nop 1
	v_add_u32_e32 v194, s13, v206
	global_load_lds_dwordx4 v194, s[18:19]
	v_add_u32_e32 v194, s13, v213
	s_mov_b32 m0, s40
	s_nop 0
	global_load_lds_dwordx4 v194, s[18:19]
	s_mov_b32 m0, s41
	v_add_u32_e32 v194, 0x90000, v129
	global_load_lds_dwordx4 v194, s[10:11]
	v_add_u32_e32 v194, 0xd8000, v129
	s_mov_b32 m0, s42
	s_nop 0
	global_load_lds_dwordx4 v194, s[10:11]
	s_setprio 0
	s_waitcnt vmcnt(8) lgkmcnt(0)
	s_barrier
	s_setprio 1
	v_mfma_f32_16x16x32_f16 v[12:15], v[130:133], v[146:149], v[12:15]
	v_mfma_f32_16x16x32_f16 v[8:11], v[138:141], v[146:149], v[8:11]
	v_mfma_f32_16x16x32_f16 v[4:7], v[130:133], v[154:157], v[4:7]
	v_mfma_f32_16x16x32_f16 v[0:3], v[138:141], v[154:157], v[0:3]
	v_mfma_f32_16x16x32_f16 v[44:47], v[130:133], v[162:165], v[44:47]
	v_mfma_f32_16x16x32_f16 v[48:51], v[138:141], v[162:165], v[48:51]
	v_mfma_f32_16x16x32_f16 v[56:59], v[130:133], v[170:173], v[56:59]
	v_mfma_f32_16x16x32_f16 v[60:63], v[138:141], v[170:173], v[60:63]
	v_mfma_f32_16x16x32_f16 v[12:15], v[134:137], v[150:153], v[12:15]
	v_mfma_f32_16x16x32_f16 v[8:11], v[142:145], v[150:153], v[8:11]
	v_mfma_f32_16x16x32_f16 v[4:7], v[134:137], v[158:161], v[4:7]
	v_mfma_f32_16x16x32_f16 v[0:3], v[142:145], v[158:161], v[0:3]
	v_mfma_f32_16x16x32_f16 v[44:47], v[134:137], v[166:169], v[44:47]
	v_mfma_f32_16x16x32_f16 v[48:51], v[142:145], v[166:169], v[48:51]
	v_mfma_f32_16x16x32_f16 v[56:59], v[134:137], v[174:177], v[56:59]
	v_mfma_f32_16x16x32_f16 v[60:63], v[142:145], v[174:177], v[60:63]
	v_mfma_f32_16x16x32_f16 v[64:67], v[178:181], v[146:149], v[64:67]
	v_mfma_f32_16x16x32_f16 v[68:71], v[186:189], v[146:149], v[68:71]
	v_mfma_f32_16x16x32_f16 v[72:75], v[178:181], v[154:157], v[72:75]
	v_mfma_f32_16x16x32_f16 v[76:79], v[186:189], v[154:157], v[76:79]
	v_mfma_f32_16x16x32_f16 v[80:83], v[178:181], v[162:165], v[80:83]
	v_mfma_f32_16x16x32_f16 v[84:87], v[186:189], v[162:165], v[84:87]
	v_mfma_f32_16x16x32_f16 v[88:91], v[178:181], v[170:173], v[88:91]
	v_mfma_f32_16x16x32_f16 v[92:95], v[186:189], v[170:173], v[92:95]
	v_mfma_f32_16x16x32_f16 v[64:67], v[182:185], v[150:153], v[64:67]
	v_mfma_f32_16x16x32_f16 v[68:71], v[190:193], v[150:153], v[68:71]
	v_mfma_f32_16x16x32_f16 v[72:75], v[182:185], v[158:161], v[72:75]
	v_mfma_f32_16x16x32_f16 v[76:79], v[190:193], v[158:161], v[76:79]
	v_mfma_f32_16x16x32_f16 v[80:83], v[182:185], v[166:169], v[80:83]
	v_mfma_f32_16x16x32_f16 v[84:87], v[190:193], v[166:169], v[84:87]
	v_mfma_f32_16x16x32_f16 v[88:91], v[182:185], v[174:177], v[88:91]
	v_mfma_f32_16x16x32_f16 v[92:95], v[190:193], v[174:177], v[92:95]
	s_setprio 0
	s_addk_i32 s7, 0x100
	s_cmp_lt_u32 s8, 32
	s_mov_b32 s8, s9
	s_barrier
	s_cbranch_scc1 .LBB1_82
	ds_read_b128 v[132:135], v219 offset:32768
	ds_read_b128 v[136:139], v219 offset:33792
	ds_read_b128 v[140:143], v219 offset:34816
	ds_read_b128 v[144:147], v219 offset:35840
	ds_read_b128 v[128:131], v220
	ds_read_b128 v[148:151], v220 offset:1024
	ds_read_b128 v[152:155], v221
	ds_read_b128 v[156:159], v221 offset:1024
	ds_read_b128 v[188:191], v222
	ds_read_b128 v[192:195], v222 offset:1024
	ds_read_b128 v[196:199], v223
	ds_read_b128 v[200:203], v223 offset:1024
	s_setprio 2
	s_lshl_b32 s3, s50, 9
	s_add_i32 s3, s47, s3
	s_add_i32 s3, s3, 0x10380
	s_mov_b32 m0, s43
	v_add_u32_e32 v160, s3, v206
	global_load_lds_dwordx4 v160, s[18:19]
	v_add_u32_e32 v160, s3, v213
	s_mov_b32 m0, s44
	s_nop 0
	global_load_lds_dwordx4 v160, s[18:19]
	s_setprio 0
	s_waitcnt vmcnt(8)
	s_barrier
	s_waitcnt lgkmcnt(0)
	s_setprio 1
	s_waitcnt lgkmcnt(0)
	v_mfma_f32_16x16x32_f16 v[124:127], v[132:135], v[128:131], v[124:127]
	v_mfma_f32_16x16x32_f16 v[120:123], v[140:143], v[128:131], v[120:123]
	v_mfma_f32_16x16x32_f16 v[116:119], v[132:135], v[152:155], v[116:119]
	v_mfma_f32_16x16x32_f16 v[112:115], v[140:143], v[152:155], v[112:115]
	v_mfma_f32_16x16x32_f16 v[108:111], v[132:135], v[188:191], v[108:111]
	v_mfma_f32_16x16x32_f16 v[104:107], v[140:143], v[188:191], v[104:107]
	v_mfma_f32_16x16x32_f16 v[100:103], v[132:135], v[196:199], v[100:103]
	v_mfma_f32_16x16x32_f16 v[96:99], v[140:143], v[196:199], v[96:99]
	v_mfma_f32_16x16x32_f16 v[160:163], v[136:139], v[148:151], v[124:127]
	v_mfma_f32_16x16x32_f16 v[164:167], v[144:147], v[148:151], v[120:123]
	v_mfma_f32_16x16x32_f16 v[168:171], v[136:139], v[156:159], v[116:119]
	v_mfma_f32_16x16x32_f16 v[172:175], v[144:147], v[156:159], v[112:115]
	v_mfma_f32_16x16x32_f16 v[176:179], v[136:139], v[192:195], v[108:111]
	v_mfma_f32_16x16x32_f16 v[180:183], v[144:147], v[192:195], v[104:107]
	v_mfma_f32_16x16x32_f16 v[100:103], v[136:139], v[200:203], v[100:103]
	v_mfma_f32_16x16x32_f16 v[184:187], v[144:147], v[200:203], v[96:99]
	s_setprio 0
	s_barrier
	ds_read_b128 v[104:107], v219 offset:49152
	ds_read_b128 v[108:111], v219 offset:50176
	ds_read_b128 v[116:119], v219 offset:51200
	ds_read_b128 v[236:239], v219 offset:52224
	s_barrier
	s_waitcnt lgkmcnt(0)
	s_setprio 1
	s_waitcnt lgkmcnt(0)
	v_mfma_f32_16x16x32_f16 v[52:55], v[104:107], v[128:131], v[52:55]
	v_mfma_f32_16x16x32_f16 v[40:43], v[116:119], v[128:131], v[40:43]
	v_mfma_f32_16x16x32_f16 v[36:39], v[104:107], v[152:155], v[36:39]
	v_mfma_f32_16x16x32_f16 v[32:35], v[116:119], v[152:155], v[32:35]
	v_mfma_f32_16x16x32_f16 v[28:31], v[104:107], v[188:191], v[28:31]
	v_mfma_f32_16x16x32_f16 v[24:27], v[116:119], v[188:191], v[24:27]
	v_mfma_f32_16x16x32_f16 v[20:23], v[104:107], v[196:199], v[20:23]
	v_mfma_f32_16x16x32_f16 v[16:19], v[116:119], v[196:199], v[16:19]
	v_mfma_f32_16x16x32_f16 v[52:55], v[108:111], v[148:151], v[52:55]
	v_mfma_f32_16x16x32_f16 v[40:43], v[236:239], v[148:151], v[40:43]
	v_mfma_f32_16x16x32_f16 v[36:39], v[108:111], v[156:159], v[36:39]
	v_mfma_f32_16x16x32_f16 v[32:35], v[236:239], v[156:159], v[32:35]
	v_mfma_f32_16x16x32_f16 v[28:31], v[108:111], v[192:195], v[28:31]
	v_mfma_f32_16x16x32_f16 v[24:27], v[236:239], v[192:195], v[24:27]
	v_mfma_f32_16x16x32_f16 v[96:99], v[108:111], v[200:203], v[20:23]
	v_mfma_f32_16x16x32_f16 v[16:19], v[236:239], v[200:203], v[16:19]
	s_setprio 0
	s_barrier
	ds_read_b128 v[20:23], v220 offset:16384
	ds_read_b128 v[148:151], v220 offset:17408
	ds_read_b128 v[152:155], v221 offset:16384
	ds_read_b128 v[156:159], v221 offset:17408
	ds_read_b128 v[188:191], v222 offset:16384
	ds_read_b128 v[192:195], v222 offset:17408
	ds_read_b128 v[196:199], v223 offset:16384
	ds_read_b128 v[200:203], v223 offset:17408
	s_waitcnt vmcnt(4)
	s_barrier
	s_waitcnt lgkmcnt(0)
	s_setprio 1
	s_waitcnt lgkmcnt(0)
	v_mfma_f32_16x16x32_f16 v[0:3], v[140:143], v[152:155], v[0:3]
	v_mfma_f32_16x16x32_f16 v[124:127], v[144:147], v[156:159], v[0:3]
	v_mfma_f32_16x16x32_f16 v[0:3], v[132:135], v[188:191], v[44:47]
	v_mfma_f32_16x16x32_f16 v[128:131], v[136:139], v[192:195], v[0:3]
	v_mfma_f32_16x16x32_f16 v[0:3], v[140:143], v[188:191], v[48:51]
	v_mfma_f32_16x16x32_f16 v[48:51], v[144:147], v[192:195], v[0:3]
	v_mfma_f32_16x16x32_f16 v[0:3], v[132:135], v[196:199], v[56:59]
	v_mfma_f32_16x16x32_f16 v[12:15], v[132:135], v[20:23], v[12:15]
	v_mfma_f32_16x16x32_f16 v[8:11], v[140:143], v[20:23], v[8:11]
	v_mfma_f32_16x16x32_f16 v[4:7], v[132:135], v[152:155], v[4:7]
	v_mfma_f32_16x16x32_f16 v[56:59], v[136:139], v[200:203], v[0:3]
	v_mfma_f32_16x16x32_f16 v[0:3], v[140:143], v[196:199], v[60:63]
	v_mfma_f32_16x16x32_f16 v[112:115], v[136:139], v[148:151], v[12:15]
	v_mfma_f32_16x16x32_f16 v[8:11], v[144:147], v[148:151], v[8:11]
	v_mfma_f32_16x16x32_f16 v[120:123], v[136:139], v[156:159], v[4:7]
	v_mfma_f32_16x16x32_f16 v[60:63], v[144:147], v[200:203], v[0:3]
	s_setprio 0
	s_setprio 1
	v_mfma_f32_16x16x32_f16 v[0:3], v[104:107], v[20:23], v[64:67]
	v_mfma_f32_16x16x32_f16 v[132:135], v[108:111], v[148:151], v[0:3]
	v_mfma_f32_16x16x32_f16 v[0:3], v[116:119], v[20:23], v[68:71]
	v_mfma_f32_16x16x32_f16 v[136:139], v[236:239], v[148:151], v[0:3]
	v_mfma_f32_16x16x32_f16 v[0:3], v[104:107], v[152:155], v[72:75]
	v_mfma_f32_16x16x32_f16 v[140:143], v[108:111], v[156:159], v[0:3]
	v_mfma_f32_16x16x32_f16 v[0:3], v[116:119], v[152:155], v[76:79]
	v_mfma_f32_16x16x32_f16 v[144:147], v[236:239], v[156:159], v[0:3]
	v_mfma_f32_16x16x32_f16 v[0:3], v[104:107], v[188:191], v[80:83]
	v_mfma_f32_16x16x32_f16 v[80:83], v[108:111], v[192:195], v[0:3]
	v_mfma_f32_16x16x32_f16 v[0:3], v[116:119], v[188:191], v[84:87]
	v_mfma_f32_16x16x32_f16 v[148:151], v[236:239], v[192:195], v[0:3]
	v_mfma_f32_16x16x32_f16 v[0:3], v[104:107], v[196:199], v[88:91]
	v_mfma_f32_16x16x32_f16 v[152:155], v[108:111], v[200:203], v[0:3]
	v_mfma_f32_16x16x32_f16 v[0:3], v[116:119], v[196:199], v[92:95]
	v_mfma_f32_16x16x32_f16 v[156:159], v[236:239], v[200:203], v[0:3]
	s_setprio 0
	s_add_i32 s49, s49, s17
	s_cmpk_lt_i32 s49, 0x1c8
	s_cselect_b64 s[6:7], -1, 0
	s_cmpk_gt_i32 s49, 0x1c7
	s_cselect_b64 s[12:13], -1, 0
	s_and_b64 vcc, exec, s[12:13]
	s_mov_b32 s54, s2
	s_mov_b32 s53, s51
	s_mov_b32 s55, s52
	s_barrier
	s_cbranch_vccnz .LBB1_100
	s_cmpk_lt_i32 s49, 0x148
	s_cbranch_scc1 .LBB1_88
	s_cmpk_lt_u32 s49, 0x1a0
	s_cbranch_scc1 .LBB1_89
	s_cmpk_lt_u32 s49, 0x1b8
	s_cbranch_scc1 .LBB1_90
	s_cmpk_lt_u32 s49, 0x1c0
	s_cselect_b32 s47, s45, 0xfffffe40
	s_cselect_b32 s48, 3, 4
	s_mov_b32 s3, 1
	s_cmp_lt_i32 s48, 1
	s_movk_i32 s53, 0x64
	s_cbranch_scc0 .LBB1_91
	s_branch .LBB1_99
